# neighbourhood-attention ring: next-row K/V prefetch no longer waited right after issue (vmcnt(0) at step head removed; counted vmcnt(2) before the ring ds_write; vmcnt(0) once at loop entry), on top o
# baseline (speedup 1.0000x reference)
; #define LAS __attribute__((address_space(3)))
; __device__ __forceinline__ void na_ring(const Params& p, LAS unsigned char* lds, int unit) {
;     ...
;     for (int i = tid; i < 15 * 31; i += 512) btab[(i / 31) * 32 + (i % 31)] = rpb[h * 465 + i] * LOG2E;
;     const int st_row = tid >> 3, st_pc = tid & 7, st_off = st_row * 128 + ((st_pc ^ (st_row & 7)) << 4);
;     const bf16_t* kg = proj + ((size_t)b * T + st_row) * LD0 + 6144 + h * 64 + st_pc * 8;
;     const bf16_t* vg = VT + (size_t)(h * 64 + st_row) * VTLD + (size_t)b * T + st_pc * 8;
;     { u32x4 kk[8], vv[8];
; #pragma unroll
;       for (int g = 0; g < 8; ++g) { kk[g] = *(const u32x4*)(kg + (size_t)g * 64 * LD0); vv[g] = *(const u32x4*)(vg + g * 64); }
; #pragma unroll
;       for (int g = 0; g < 8; ++g) { *(LAS u32x4*)(lds + KRING + g * 8192 + st_off) = kk[g]; *(LAS u32x4*)(lds + VRING + g * 8192 + st_off) = vv[g]; } }
.LBB0_298:
	s_or_b64 exec, exec, s[4:5]
	s_ashr_i32 s48, s78, 4
	s_ashr_i32 s49, s48, 31
	v_ashrrev_i32_e32 v4, 3, v2
	s_lshl_b64 s[6:7], s[48:49], 11
	v_ashrrev_i32_e32 v5, 31, v4
	v_lshl_add_u64 v[6:7], s[6:7], 0, v[4:5]
	v_mov_b64_e32 v[78:79], s[12:13]
	v_mad_u64_u32 v[8:9], s[8:9], v6, s58, v[78:79]
	s_lshl_b32 s4, s40, 7
	v_mad_i32_i24 v9, v7, s58, v9
	s_mov_b32 s5, s41
	v_lshlrev_b32_e32 v0, 4, v2
	v_lshl_add_u64 v[6:7], v[8:9], 0, s[4:5]
	v_and_b32_e32 v54, 0x70, v0
	v_lshl_add_u64 v[68:69], v[6:7], 0, v[54:55]
	v_lshl_add_u32 v0, s40, 6, v4
	v_mov_b64_e32 v[6:7], s[10:11]
	s_lshl_b64 s[50:51], s[48:49], 12
	v_mad_i64_i32 v[6:7], s[8:9], v0, s61, v[6:7]
	v_lshl_add_u64 v[6:7], v[6:7], 0, s[50:51]
	v_lshl_add_u64 v[74:75], v[6:7], 0, v[54:55]
	v_add_co_u32_e32 v6, vcc, s62, v68
	s_and_b32 s8, s77, 15
	s_nop 0
	v_addc_co_u32_e32 v7, vcc, 0, v69, vcc
	v_add_co_u32_e32 v10, vcc, s63, v68
	v_xor_b32_e32 v3, v4, v2
	s_nop 0
	v_addc_co_u32_e32 v11, vcc, 0, v69, vcc
	v_add_co_u32_e32 v22, vcc, s64, v68
	global_load_dwordx4 v[6:9], v[6:7], off
	s_nop 0
	global_load_dwordx4 v[10:13], v[10:11], off
	s_nop 0
	global_load_dwordx4 v[14:17], v[74:75], off
	global_load_dwordx4 v[18:21], v[74:75], off offset:128
	v_addc_co_u32_e32 v23, vcc, 0, v69, vcc
	v_add_co_u32_e32 v26, vcc, s65, v68
	s_mul_i32 s85, s8, 0x202000
	s_nop 0
	v_addc_co_u32_e32 v27, vcc, 0, v69, vcc
	v_add_co_u32_e32 v38, vcc, s71, v68
	global_load_dwordx4 v[22:25], v[22:23], off
	s_nop 0
	global_load_dwordx4 v[26:29], v[26:27], off
	s_nop 0
	global_load_dwordx4 v[30:33], v[74:75], off offset:256
	global_load_dwordx4 v[34:37], v[74:75], off offset:384
	v_addc_co_u32_e32 v39, vcc, 0, v69, vcc
	v_add_co_u32_e32 v42, vcc, s72, v68
	s_lshl_b32 s40, s8, 7
	s_nop 0
	v_addc_co_u32_e32 v43, vcc, 0, v69, vcc
	v_add_co_u32_e32 v56, vcc, s73, v68
	global_load_dwordx4 v[38:41], v[38:39], off
	s_nop 0
	global_load_dwordx4 v[42:45], v[42:43], off
	s_nop 0
	global_load_dwordx4 v[46:49], v[74:75], off offset:512
	global_load_dwordx4 v[50:53], v[74:75], off offset:640
	v_addc_co_u32_e32 v57, vcc, 0, v69, vcc
	v_add_co_u32_e32 v68, vcc, s74, v68
	global_load_dwordx4 v[56:59], v[56:57], off
	s_nop 0
	global_load_dwordx4 v[60:63], v[74:75], off offset:768
	v_addc_co_u32_e32 v69, vcc, 0, v69, vcc
	global_load_dwordx4 v[70:73], v[68:69], off
	s_nop 0
	global_load_dwordx4 v[74:77], v[74:75], off offset:896
	s_lshl_b32 s84, s8, 6
	s_bfe_u32 s8, s79, 0x20006
	v_lshlrev_b32_e32 v3, 4, v3
	v_lshlrev_b32_e32 v54, 7, v4
	s_lshl_b32 s81, s8, 4
	s_mul_i32 s9, s8, 0xa00
	v_and_or_b32 v3, v3, s59, v54
	v_and_b32_e32 v5, 15, v2
	s_ashr_i32 s49, s79, 8
	s_or_b32 s6, s6, s81
	s_add_i32 s9, s9, 0
	v_add_u32_e32 v67, 0, v3
	s_add_i32 s82, s9, 0x24000
	s_lshl_b32 s79, s49, 2
	v_add_u32_e32 v68, s57, v3
	s_cmp_gt_u32 s8, 1
	v_and_b32_e32 v54, 48, v2
	v_and_b32_e32 v0, 63, v2
	v_bfe_u32 v80, v2, 4, 2
	v_lshl_add_u32 v69, v0, 2, s82
	v_lshlrev_b32_e32 v0, 7, v5
	s_cselect_b32 s86, 2, 1
	v_add_u32_e32 v100, s57, v0
	s_mov_b32 s80, 0
	s_waitcnt vmcnt(15)
	ds_write_b128 v67, v[6:9]
	s_waitcnt vmcnt(13)
	ds_write_b128 v68, v[14:17]
	ds_write_b128 v67, v[10:13] offset:8192
	s_waitcnt vmcnt(12)
	ds_write_b128 v68, v[18:21] offset:8192
	s_waitcnt vmcnt(11)
	ds_write_b128 v67, v[22:25] offset:16384
	s_waitcnt vmcnt(9)
	ds_write_b128 v68, v[30:33] offset:16384
	ds_write_b128 v67, v[26:29] offset:24576
	s_waitcnt vmcnt(8)
	ds_write_b128 v68, v[34:37] offset:24576
	s_waitcnt vmcnt(7)
	ds_write_b128 v67, v[38:41] offset:32768
	s_waitcnt vmcnt(5)
	ds_write_b128 v68, v[46:49] offset:32768
	ds_write_b128 v67, v[42:45] offset:40960
	s_waitcnt vmcnt(4)
	ds_write_b128 v68, v[50:53] offset:40960
	s_waitcnt vmcnt(3)
	ds_write_b128 v67, v[56:59] offset:49152
	s_waitcnt vmcnt(2)
	ds_write_b128 v68, v[60:63] offset:49152
	s_waitcnt vmcnt(1)
	ds_write_b128 v67, v[70:73] offset:57344
	s_waitcnt vmcnt(0)
; #define LAS __attribute__((address_space(3)))
; __device__ __forceinline__ void na_ring(const Params& p, LAS unsigned char* lds, int unit) {
;     ...
;       for (int g = 0; g < 8; ++g) { *(LAS u32x4*)(lds + KRING + g * 8192 + st_off) = kk[g]; *(LAS u32x4*)(lds + VRING + g * 8192 + st_off) = vv[g]; } }
;     const bf16_t* qg = proj + ((size_t)b * T + 16 * qb + fr) * LD0 + 5120 + h * 64 + 8 * fq;
;     bf16x8 qf[2]; qf[0] = *(const bf16x8*)qg; qf[1] = *(const bf16x8*)(qg + 32);
;     const int c = 16 * qb + fr, cs = min(max(c - 8, 0), 48);
;     LAS unsigned* mb = (LAS unsigned*)(lds + MERGE) + qb * 640 + lane;
;     __syncthreads();
;     for (int r = 0; r < 32; ++r) {
;         const int r0 = min(max(r - 4, 0), 24);
;         const bool pf = (r >= 4) && (r < 28);
;         u32x4 pk_ = {0u, 0u, 0u, 0u}, pv_ = {0u, 0u, 0u, 0u};
;         if (pf) { pk_ = *(const u32x4*)(kg + (size_t)(r + 4) * 64 * LD0); pv_ = *(const u32x4*)(vg + (r + 4) * 64); }
;         bf16x8 qn0 = qf[0], qn1 = qf[1];
;         if (r + 1 < 32) { qn0 = *(const bf16x8*)(qg + (size_t)(r + 1) * 64 * LD0); qn1 = *(const bf16x8*)(qg + (size_t)(r + 1) * 64 * LD0 + 32); }
;         f32x4 sc[12];
;         int slot[4];
; #pragma unroll
;         for (int k4 = 0; k4 < 4; ++k4) { slot[k4] = (r0 + 4 * hf + k4) % 9;
;             const LAS unsigned char* ks = lds + KRING + slot[k4] * 8192;
; #pragma unroll
;             for (int cbi = 0; cbi < 3; ++cbi) { const int tok = 16 * (cb0 + cbi) + fr;
;                 const bf16x8 a0 = *(const LAS bf16x8*)(ks + tok * 128 + ((fq ^ (tok & 7)) << 4)), a1 = *(const LAS bf16x8*)(ks + tok * 128 + (((4 + fq) ^ (tok & 7)) << 4));
;                 f32x4 a = {0.f, 0.f, 0.f, 0.f};
;                 a = __builtin_amdgcn_mfma_f32_16x16x32_bf16(a0, qf[0], a, 0, 0, 0);
;                 a = __builtin_amdgcn_mfma_f32_16x16x32_bf16(a1, qf[1], a, 0, 0, 0);
;                 sc[k4 * 3 + cbi] = a; } }
;         float mx = -1e30f;
; #pragma unroll
;         for (int k4 = 0; k4 < 4; ++k4) { const LAS float* bt = btab + (r0 + 4 * hf + k4 - r + 7) * 32;
; #pragma unroll
;             for (int cbi = 0; cbi < 3; ++cbi)
; #pragma unroll
;                 for (int j = 0; j < 4; ++j) { const int sidx = 16 * (cb0 + cbi) + 4 * fq + j; const bool ok = (sidx >= cs) && (sidx < cs + 16);
;                     const int dc = min(max(sidx - c + 15, 0), 30);
	ds_write_b128 v68, v[74:77] offset:57344
	v_or_b32_e32 v6, s6, v5
	v_mad_u64_u32 v[10:11], s[8:9], v6, s58, v[78:79]
	v_mad_i32_i24 v11, s7, v1, v11
	v_lshl_add_u64 v[10:11], v[10:11], 0, s[4:5]
	v_lshl_add_u64 v[10:11], v[10:11], 0, v[54:55]
	v_lshl_add_u64 v[12:13], v[10:11], 0, s[42:43]
	v_add_co_u32_e32 v10, vcc, s75, v10
	v_and_b32_e32 v15, 64, v64
	s_nop 0
	v_addc_co_u32_e32 v11, vcc, 0, v11, vcc
	global_load_dwordx4 v[22:25], v[10:11], off offset:2048
	global_load_dwordx4 v[18:21], v[12:13], off offset:64
	v_xor_b32_e32 v14, 16, v64
	v_add_u32_e32 v15, 64, v15
	v_cmp_lt_i32_e32 vcc, v14, v15
	v_or_b32_e32 v10, s81, v5
	v_and_b32_e32 v5, 7, v2
	v_bitop3_b32 v12, v80, v2, 7 bitop3:0x78
	v_cndmask_b32_e32 v14, v64, v14, vcc
	s_mul_i32 s6, s7, 0x4080
	v_mad_u64_u32 v[8:9], s[8:9], v6, s58, 0
	v_lshlrev_b32_e32 v71, 4, v12
	v_bitop3_b32 v12, v80, v5, 4 bitop3:0x36
	v_lshlrev_b32_e32 v73, 2, v14
	v_xor_b32_e32 v14, 32, v64
	v_add_u32_e32 v3, s6, v9
	v_lshrrev_b32_e32 v9, 1, v2
	v_lshlrev_b32_e32 v72, 4, v12
	v_lshlrev_b32_e32 v12, 2, v80
	v_cmp_lt_i32_e32 vcc, v14, v15
	s_cselect_b32 s4, 3, 2
	v_and_b32_e32 v75, 8, v9
	v_cndmask_b32_e32 v14, v64, v14, vcc
	v_lshl_or_b32 v9, s4, 4, v12
	v_lshlrev_b32_e32 v74, 2, v14
	v_sub_u32_e32 v14, v9, v10
	v_max_i32_e32 v14, -15, v14
	s_cselect_b32 s6, 16, 0
	v_add_u32_e32 v14, 15, v14
	v_sub_u32_e64 v11, v10, 8 clamp
	v_min_u32_e32 v76, 30, v14
	v_or_b32_e32 v14, s6, v12
	v_min_u32_e32 v11, 48, v11
	v_sub_u32_e32 v15, v14, v10
	v_add_u32_e32 v13, 16, v11
	v_max_i32_e32 v15, -15, v15
	v_mov_b32_e32 v7, s7
	v_cmp_ge_u32_e64 s[6:7], v14, v11
	v_cmp_lt_u32_e64 s[8:9], v14, v13
	v_add_u32_e32 v15, 15, v15
	s_cselect_b32 s81, 0x800, 0
	v_min_u32_e32 v77, 30, v15
	s_and_b64 s[6:7], s[6:7], s[8:9]
	v_or_b32_e32 v15, 1, v14
	v_cndmask_b32_e64 v78, v65, 0, s[6:7]
	v_cmp_ge_u32_e64 s[6:7], v15, v11
	v_cmp_lt_u32_e64 s[8:9], v15, v13
	v_sub_u32_e32 v15, v15, v10
	v_max_i32_e32 v15, -15, v15
	v_add_u32_e32 v15, 15, v15
	v_min_u32_e32 v79, 30, v15
	s_and_b64 s[6:7], s[6:7], s[8:9]
	v_or_b32_e32 v15, 2, v14
	v_cndmask_b32_e64 v80, v65, 0, s[6:7]
	v_cmp_ge_u32_e64 s[6:7], v15, v11
	v_cmp_lt_u32_e64 s[8:9], v15, v13
	v_sub_u32_e32 v15, v15, v10
	v_max_i32_e32 v15, -15, v15
	v_add_u32_e32 v15, 15, v15
	v_min_u32_e32 v81, 30, v15
	s_and_b64 s[6:7], s[6:7], s[8:9]
	v_or_b32_e32 v15, 3, v14
	v_cndmask_b32_e64 v82, v65, 0, s[6:7]
	v_cmp_ge_u32_e64 s[6:7], v15, v11
	v_cmp_lt_u32_e64 s[8:9], v15, v13
	v_sub_u32_e32 v15, v15, v10
	v_max_i32_e32 v15, -15, v15
	v_add_u32_e32 v15, 15, v15
	v_min_u32_e32 v83, 30, v15
	v_lshl_or_b32 v15, s86, 4, v12
	v_sub_u32_e32 v16, v15, v10
	s_and_b64 s[6:7], s[6:7], s[8:9]
	v_max_i32_e32 v16, -15, v16
	v_cndmask_b32_e64 v84, v65, 0, s[6:7]
	v_cmp_ge_u32_e64 s[6:7], v15, v11
	v_cmp_lt_u32_e64 s[8:9], v15, v13
	v_add_u32_e32 v16, 15, v16
	v_min_u32_e32 v85, 30, v16
	s_and_b64 s[6:7], s[6:7], s[8:9]
	v_or_b32_e32 v16, 1, v15
	v_cndmask_b32_e64 v86, v65, 0, s[6:7]
	v_cmp_ge_u32_e64 s[6:7], v16, v11
	v_cmp_lt_u32_e64 s[8:9], v16, v13
	v_sub_u32_e32 v16, v16, v10
	v_max_i32_e32 v16, -15, v16
	v_add_u32_e32 v16, 15, v16
	v_min_u32_e32 v87, 30, v16
	s_and_b64 s[6:7], s[6:7], s[8:9]
	v_or_b32_e32 v16, 2, v15
	v_cndmask_b32_e64 v88, v65, 0, s[6:7]
	v_cmp_ge_u32_e64 s[6:7], v16, v11
	v_cmp_lt_u32_e64 s[8:9], v16, v13
	v_sub_u32_e32 v16, v16, v10
	v_max_i32_e32 v16, -15, v16
	v_add_u32_e32 v16, 15, v16
	v_min_u32_e32 v89, 30, v16
	s_and_b64 s[6:7], s[6:7], s[8:9]
	v_or_b32_e32 v16, 3, v15
	v_cndmask_b32_e64 v90, v65, 0, s[6:7]
	v_cmp_ge_u32_e64 s[6:7], v16, v11
	v_cmp_lt_u32_e64 s[8:9], v16, v13
	v_sub_u32_e32 v16, v16, v10
	v_max_i32_e32 v16, -15, v16
	s_lshl_b32 s83, s4, 11
	v_cmp_ge_u32_e32 vcc, v9, v11
	v_cmp_lt_u32_e64 s[4:5], v9, v13
	v_add_u32_e32 v16, 15, v16
	v_min_u32_e32 v91, 30, v16
	s_and_b64 s[4:5], vcc, s[4:5]
	v_or_b32_e32 v16, 1, v9
	v_cndmask_b32_e64 v93, v65, 0, s[4:5]
	v_cmp_ge_u32_e32 vcc, v16, v11
	v_cmp_lt_u32_e64 s[4:5], v16, v13
	v_sub_u32_e32 v16, v16, v10
	v_max_i32_e32 v16, -15, v16
	v_add_u32_e32 v16, 15, v16
	v_min_u32_e32 v94, 30, v16
	s_and_b64 s[4:5], vcc, s[4:5]
	v_or_b32_e32 v16, 2, v9
	v_cndmask_b32_e64 v95, v65, 0, s[4:5]
	v_cmp_ge_u32_e32 vcc, v16, v11
	v_cmp_lt_u32_e64 s[4:5], v16, v13
	v_sub_u32_e32 v16, v16, v10
	v_max_i32_e32 v16, -15, v16
	v_add_u32_e32 v16, 15, v16
	v_add_u32_e32 v70, 0, v0
	v_min_u32_e32 v96, 30, v16
	s_and_b64 s[4:5], vcc, s[4:5]
	v_or_b32_e32 v16, 3, v9
	v_lshrrev_b32_e32 v0, 3, v14
	v_cndmask_b32_e64 v97, v65, 0, s[4:5]
	v_cmp_ge_u32_e32 vcc, v16, v11
	v_cmp_lt_u32_e64 s[4:5], v16, v13
	v_bitop3_b32 v0, v0, v2, 7 bitop3:0x78
	s_lshl_b32 s82, s86, 11
	s_and_b64 s[6:7], s[6:7], s[8:9]
	v_sub_u32_e32 v10, v16, v10
	s_and_b64 s[4:5], vcc, s[4:5]
	v_lshlrev_b32_e32 v101, 4, v0
	v_lshrrev_b32_e32 v0, 3, v15
	v_max_i32_e32 v10, -15, v10
	v_cndmask_b32_e64 v99, v65, 0, s[4:5]
	v_bitop3_b32 v0, v0, v2, 7 bitop3:0x78
	s_add_u32 s4, s50, s85
	v_add_u32_e32 v10, 15, v10
	v_lshlrev_b32_e32 v102, 4, v0
	v_lshrrev_b32_e32 v0, 3, v9
	s_addc_u32 s5, s51, 0
	v_min_u32_e32 v98, 30, v10
	v_bitop3_b32 v0, v0, v2, 7 bitop3:0x78
	v_mov_b64_e32 v[10:11], s[4:5]
	v_lshlrev_b32_e32 v103, 4, v0
	v_mad_i64_i32 v[10:11], s[4:5], v4, s61, v[10:11]
	v_lshlrev_b32_e32 v0, 4, v5
	v_mad_i64_i32 v[4:5], s[4:5], v4, s58, 0
	v_mad_i64_i32 v[4:5], s[4:5], s48, v66, v[4:5]
	v_or_b32_e32 v4, v4, v0
	v_lshl_add_u64 v[58:59], s[36:37], 0, v[4:5]
	v_lshlrev_b64 v[4:5], 11, v[6:7]
	v_or_b32_e32 v10, v10, v0
	v_or3_b32 v4, v4, s84, v12
	v_or_b32_e32 v2, v8, v54
	v_cndmask_b32_e64 v92, v65, 0, s[6:7]
	v_lshl_add_u64 v[56:57], s[18:19], 0, v[10:11]
	v_lshl_add_u64 v[60:61], s[14:15], 0, v[4:5]
	v_lshl_add_u64 v[62:63], s[12:13], 0, v[2:3]
	s_mov_b32 s48, -4
	s_mov_b64 s[4:5], 0
	s_mov_b32 s50, s79
	s_waitcnt vmcnt(0) lgkmcnt(0)
	s_barrier
	s_branch .LBB0_300

; __device__ __forceinline__ void na_ring(const Params& p, LAS unsigned char* lds, int unit) {
;     ...
;         u32x4 pk_ = {0u, 0u, 0u, 0u}, pv_ = {0u, 0u, 0u, 0u};
;         if (pf) { pk_ = *(const u32x4*)(kg + (size_t)(r + 4) * 64 * LD0); pv_ = *(const u32x4*)(vg + (r + 4) * 64); }
;         bf16x8 qn0 = qf[0], qn1 = qf[1];
;         if (r + 1 < 32) { qn0 = *(const bf16x8*)(qg + (size_t)(r + 1) * 64 * LD0); qn1 = *(const bf16x8*)(qg + (size_t)(r + 1) * 64 * LD0 + 32); }
.LBB0_302:
	v_mov_b64_e32 v[6:7], v[18:19]
	v_mov_b64_e32 v[2:3], v[22:23]
	s_cmp_eq_u32 s4, 0x3e0000
	v_mov_b64_e32 v[8:9], v[20:21]
	v_mov_b64_e32 v[4:5], v[24:25]
	s_cbranch_scc1 .LBB0_304
	v_lshl_add_u64 v[2:3], v[62:63], 0, s[40:41]
	v_add_co_u32_e32 v6, vcc, 0x104000, v2
	s_nop 1
	v_addc_co_u32_e32 v7, vcc, 0, v3, vcc
	global_load_dwordx4 v[2:5], v[6:7], off offset:2048
	s_nop 0
	global_load_dwordx4 v[6:9], v[6:7], off offset:2112

; #define LAS __attribute__((address_space(3)))
; __device__ __forceinline__ void na_ring(const Params& p, LAS unsigned char* lds, int unit) {
;     ...
;         if (pf) { const int sl = (r + 4) % 9; *(LAS u32x4*)(lds + KRING + sl * 8192 + st_off) = pk_; *(LAS u32x4*)(lds + VRING + sl * 8192 + st_off) = pv_; }
.LBB0_306:
	s_andn2_b64 vcc, exec, s[6:7]
	s_cbranch_vccnz .LBB0_308
	s_add_i32 s6, s80, 4
	s_and_b32 s7, s6, 0xff
	s_mul_i32 s7, s7, 57
	s_bfe_u32 s7, s7, 0x70009
	s_mul_i32 s7, s7, 9
	s_sub_i32 s6, s6, s7
	s_and_b32 s6, s6, 0xff
	s_lshl_b32 s6, s6, 13
	v_add_u32_e32 v0, s6, v67
	s_waitcnt vmcnt(2)
	ds_write_b128 v0, v[14:17]
	v_add_u32_e32 v0, s6, v68
	ds_write_b128 v0, v[10:13]
